# baseline (speedup 1.0000x reference)
_Z6attn_kPKDF16_S0_S0_PKfPDF16_PK15HIP_vector_typeIfLj4EEiPf:
	v_lshlrev_b32_e32 v117, 4, v0
	s_getpc_b64 s[92:93]
	s_add_u32 s92, s92, 0xacf8
	s_addc_u32 s93, s93, 0x0
	global_load_dword v118, v117, s[92:93]
	s_cmpk_lt_u32 s2, 0xc0
	s_mov_b64 s[4:5], -1
	s_cbranch_scc0 .LBB5_6
	s_load_dwordx8 s[4:11], s[0:1], 0x0
	s_and_b32 s3, s2, 7
	s_mul_i32 s3, s3, 12
	s_lshr_b32 s12, s2, 4
	s_add_i32 s3, s3, s12
	s_mul_i32 s12, s3, 0xab
	s_bfe_u32 s12, s12, 0x5000b
	s_lshl_b32 s13, s3, 16
	s_lshl_b32 s14, s12, 9
	v_lshlrev_b32_e32 v2, 4, v0
	v_mov_b32_e32 v3, 0
	v_or_b32_e32 v4, s14, v0
	v_lshlrev_b32_e32 v4, 2, v4
	v_lshrrev_b32_e32 v1, 6, v0
	v_and_b32_e32 v49, 63, v0
	s_nop 0
	v_readfirstlane_b32 s15, v1
	v_and_or_b32 v1, s2, 8, v1
	v_lshlrev_b32_e32 v83, 4, v49
	v_lshl_or_b32 v49, v1, 12, v83
	s_lshl_b32 s15, s15, 10
	s_mov_b64 s[16:17], 0x2000
	s_waitcnt lgkmcnt(0)
	s_add_u32 s6, s6, s13
	s_addc_u32 s7, s7, 0
	s_add_u32 s8, s8, s13
	s_addc_u32 s9, s9, 0
	s_add_u32 s4, s4, s13
	s_addc_u32 s5, s5, 0
	v_lshl_add_u64 v[112:113], s[6:7], 0, v[2:3]
	v_lshl_add_u64 v[114:115], s[8:9], 0, v[2:3]
	s_add_i32 s18, s15, 0x0
	s_mov_b32 m0, s18
	s_add_i32 s18, s15, 0x10000
	global_load_lds_dwordx4 v[112:113], off
	s_mov_b32 m0, s18
	v_lshl_add_u64 v[112:113], v[112:113], 0, s[16:17]
	global_load_lds_dwordx4 v[114:115], off
	v_lshl_add_u64 v[114:115], v[114:115], 0, s[16:17]
	s_add_i32 s18, s15, 0x2000
	s_mov_b32 m0, s18
	s_add_i32 s18, s15, 0x12000
	global_load_lds_dwordx4 v[112:113], off
	s_mov_b32 m0, s18
	v_lshl_add_u64 v[112:113], v[112:113], 0, s[16:17]
	global_load_lds_dwordx4 v[114:115], off
	v_lshl_add_u64 v[114:115], v[114:115], 0, s[16:17]
	s_add_i32 s18, s15, 0x4000
	s_mov_b32 m0, s18
	s_add_i32 s18, s15, 0x14000
	global_load_lds_dwordx4 v[112:113], off
	s_mov_b32 m0, s18
	v_lshl_add_u64 v[112:113], v[112:113], 0, s[16:17]
	global_load_lds_dwordx4 v[114:115], off
	v_lshl_add_u64 v[114:115], v[114:115], 0, s[16:17]
	s_add_i32 s18, s15, 0x6000
	s_mov_b32 m0, s18
	s_add_i32 s18, s15, 0x16000
	global_load_lds_dwordx4 v[112:113], off
	s_mov_b32 m0, s18
	v_lshl_add_u64 v[112:113], v[112:113], 0, s[16:17]
	global_load_lds_dwordx4 v[114:115], off
	v_lshl_add_u64 v[114:115], v[114:115], 0, s[16:17]
	s_add_i32 s18, s15, 0x8000
	s_mov_b32 m0, s18
	s_add_i32 s18, s15, 0x18000
	global_load_lds_dwordx4 v[112:113], off
	s_mov_b32 m0, s18
	v_lshl_add_u64 v[112:113], v[112:113], 0, s[16:17]
	global_load_lds_dwordx4 v[114:115], off
	v_lshl_add_u64 v[114:115], v[114:115], 0, s[16:17]
	s_add_i32 s18, s15, 0xa000
	s_mov_b32 m0, s18
	s_add_i32 s18, s15, 0x1a000
	global_load_lds_dwordx4 v[112:113], off
	s_mov_b32 m0, s18
	v_lshl_add_u64 v[112:113], v[112:113], 0, s[16:17]
	global_load_lds_dwordx4 v[114:115], off
	v_lshl_add_u64 v[114:115], v[114:115], 0, s[16:17]
	s_add_i32 s18, s15, 0xc000
	s_mov_b32 m0, s18
	s_add_i32 s18, s15, 0x1c000
	global_load_lds_dwordx4 v[112:113], off
	s_mov_b32 m0, s18
	v_lshl_add_u64 v[112:113], v[112:113], 0, s[16:17]
	global_load_lds_dwordx4 v[114:115], off
	v_lshl_add_u64 v[114:115], v[114:115], 0, s[16:17]
	s_add_i32 s18, s15, 0xe000
	s_mov_b32 m0, s18
	s_add_i32 s18, s15, 0x1e000
	global_load_lds_dwordx4 v[112:113], off
	s_mov_b32 m0, s18
	v_lshl_add_u64 v[112:113], v[112:113], 0, s[16:17]
	global_load_lds_dwordx4 v[114:115], off
	v_lshl_add_u64 v[114:115], v[114:115], 0, s[16:17]
	global_load_dword v48, v4, s[10:11]
	global_load_dwordx4 v[50:53], v49, s[4:5]
	global_load_dwordx4 v[54:57], v49, s[4:5] offset:1024
	global_load_dwordx4 v[58:61], v49, s[4:5] offset:2048
	global_load_dwordx4 v[62:65], v49, s[4:5] offset:3072
	s_load_dwordx2 s[6:7], s[0:1], 0x20
	s_lshl_b32 s8, s12, 9
	v_bfe_u32 v82, v0, 5, 1
	s_mov_b32 s9, 16
	s_mov_b32 s10, 0x41000000
	v_mov_b32_e32 v116, 0x20000
	v_lshl_or_b32 v116, v0, 2, v116
	v_and_b32_e32 v2, 32, v0
	v_cmp_eq_u32_e32 vcc, 0, v2
	v_mov_b32_e32 v2, 0
	v_mov_b32_e32 v3, 0
	v_mov_b32_e32 v4, 0
	v_mov_b32_e32 v5, 0
	v_mov_b32_e32 v6, 0
	v_mov_b32_e32 v7, 0
	v_mov_b32_e32 v8, 0
	v_mov_b32_e32 v9, 0
	v_mov_b32_e32 v10, 0
	v_mov_b32_e32 v11, 0
	v_mov_b32_e32 v12, 0
	v_mov_b32_e32 v13, 0
	v_mov_b32_e32 v14, 0
	v_mov_b32_e32 v15, 0
	v_mov_b32_e32 v16, 0
	v_mov_b32_e32 v17, 0
	v_mov_b32_e32 v18, 0
	v_mov_b32_e32 v19, 0
	v_mov_b32_e32 v20, 0
	v_mov_b32_e32 v21, 0
	v_mov_b32_e32 v22, 0
	v_mov_b32_e32 v23, 0
	v_mov_b32_e32 v24, 0
	v_mov_b32_e32 v25, 0
	v_mov_b32_e32 v26, 0
	v_mov_b32_e32 v27, 0
	v_mov_b32_e32 v28, 0
	v_mov_b32_e32 v29, 0
	v_mov_b32_e32 v30, 0
	v_mov_b32_e32 v31, 0
	v_mov_b32_e32 v32, 0
	v_mov_b32_e32 v33, 0
	v_lshlrev_b32_e32 v84, 4, v82
	v_mov_b32_e32 v86, 0xf149f2ca
	v_mov_b32_e32 v85, 0
	s_waitcnt vmcnt(4)
	ds_write_b32 v116, v48
	s_waitcnt lgkmcnt(0)
	s_barrier
	s_branch .LBB5_3

	.amdhsa_kernel _Z6attn_kPKDF16_S0_S0_PKfPDF16_PK15HIP_vector_typeIfLj4EEiPf
		.amdhsa_group_segment_fixed_size 133120
		.amdhsa_private_segment_fixed_size 0
		.amdhsa_kernarg_size 64
		.amdhsa_user_sgpr_count 2
		.amdhsa_user_sgpr_dispatch_ptr 0
		.amdhsa_user_sgpr_queue_ptr 0
		.amdhsa_user_sgpr_kernarg_segment_ptr 1
		.amdhsa_user_sgpr_dispatch_id 0
		.amdhsa_user_sgpr_kernarg_preload_length 0
		.amdhsa_user_sgpr_kernarg_preload_offset 0
		.amdhsa_user_sgpr_private_segment_size 0
		.amdhsa_uses_dynamic_stack 0
		.amdhsa_enable_private_segment 0
		.amdhsa_system_sgpr_workgroup_id_x 1
		.amdhsa_system_sgpr_workgroup_id_y 0
		.amdhsa_system_sgpr_workgroup_id_z 0
		.amdhsa_system_sgpr_workgroup_info 0
		.amdhsa_system_vgpr_workitem_id 0
		.amdhsa_next_free_vgpr 169
		.amdhsa_next_free_sgpr 96
		.amdhsa_accum_offset 120
		.amdhsa_reserve_vcc 1
		.amdhsa_float_round_mode_32 0
		.amdhsa_float_round_mode_16_64 0
		.amdhsa_float_denorm_mode_32 3
		.amdhsa_float_denorm_mode_16_64 3
		.amdhsa_dx10_clamp 1
		.amdhsa_ieee_mode 1
		.amdhsa_fp16_overflow 0
		.amdhsa_tg_split 0
		.amdhsa_exception_fp_ieee_invalid_op 0
		.amdhsa_exception_fp_denorm_src 0
		.amdhsa_exception_fp_ieee_div_zero 0
		.amdhsa_exception_fp_ieee_overflow 0
		.amdhsa_exception_fp_ieee_underflow 0
		.amdhsa_exception_fp_ieee_inexact 0
		.amdhsa_exception_int_div_zero 0
	.end_amdhsa_kernel

amdhsa.kernels:
  - .agpr_count:     0
    .args:
      - .address_space:  global
        .offset:         0
        .size:           8
        .value_kind:     global_buffer
    .group_segment_fixed_size: 0
    .kernarg_segment_align: 8
    .kernarg_segment_size: 8
    .language:       OpenCL C
    .language_version:
      - 2
      - 0
    .max_flat_workgroup_size: 1024
    .name:           _Z7empty_kPi
    .private_segment_fixed_size: 0
    .sgpr_count:     6
    .sgpr_spill_count: 0
    .symbol:         _Z7empty_kPi.kd
    .uniform_work_group_size: 1
    .uses_dynamic_stack: false
    .vgpr_count:     0
    .vgpr_spill_count: 0
    .wavefront_size: 64
  - .agpr_count:     0
    .args:
      - .actual_access:  read_only
        .address_space:  global
        .offset:         0
        .size:           8
        .value_kind:     global_buffer
      - .actual_access:  read_only
        .address_space:  global
        .offset:         8
        .size:           8
        .value_kind:     global_buffer
      - .actual_access:  read_only
        .address_space:  global
        .offset:         16
        .size:           8
        .value_kind:     global_buffer
      - .actual_access:  read_only
        .address_space:  global
        .offset:         24
        .size:           8
        .value_kind:     global_buffer
      - .actual_access:  write_only
        .address_space:  global
        .offset:         32
        .size:           8
        .value_kind:     global_buffer
      - .actual_access:  write_only
        .address_space:  global
        .offset:         40
        .size:           8
        .value_kind:     global_buffer
    .group_segment_fixed_size: 0
    .kernarg_segment_align: 8
    .kernarg_segment_size: 48
    .language:       OpenCL C
    .language_version:
      - 2
      - 0
    .max_flat_workgroup_size: 256
    .name:           _Z4ln_kPKfS0_S0_S0_PfPDF16_
    .private_segment_fixed_size: 0
    .sgpr_count:     22
    .sgpr_spill_count: 0
    .symbol:         _Z4ln_kPKfS0_S0_S0_PfPDF16_.kd
    .uniform_work_group_size: 1
    .uses_dynamic_stack: false
    .vgpr_count:     61
    .vgpr_spill_count: 0
    .wavefront_size: 64
  - .agpr_count:     0
    .args:
      - .actual_access:  read_only
        .address_space:  global
        .offset:         0
        .size:           8
        .value_kind:     global_buffer
      - .actual_access:  read_only
        .address_space:  global
        .offset:         8
        .size:           8
        .value_kind:     global_buffer
      - .actual_access:  read_only
        .address_space:  global
        .offset:         16
        .size:           8
        .value_kind:     global_buffer
      - .actual_access:  read_only
        .address_space:  global
        .offset:         24
        .size:           8
        .value_kind:     global_buffer
      - .actual_access:  read_only
        .address_space:  global
        .offset:         32
        .size:           8
        .value_kind:     global_buffer
      - .actual_access:  write_only
        .address_space:  global
        .offset:         40
        .size:           8
        .value_kind:     global_buffer
      - .actual_access:  write_only
        .address_space:  global
        .offset:         48
        .size:           8
        .value_kind:     global_buffer
      - .actual_access:  write_only
        .address_space:  global
        .offset:         56
        .size:           8
        .value_kind:     global_buffer
      - .actual_access:  write_only
        .address_space:  global
        .offset:         64
        .size:           8
        .value_kind:     global_buffer
      - .offset:         72
        .size:           4
        .value_kind:     by_value
    .group_segment_fixed_size: 24704
    .kernarg_segment_align: 8
    .kernarg_segment_size: 76
    .language:       OpenCL C
    .language_version:
      - 2
      - 0
    .max_flat_workgroup_size: 1024
    .name:           _Z11ln_router_kPKfS0_S0_S0_S0_PfPDF16_PiS1_i
    .private_segment_fixed_size: 0
    .sgpr_count:     36
    .sgpr_spill_count: 0
    .symbol:         _Z11ln_router_kPKfS0_S0_S0_S0_PfPDF16_PiS1_i.kd
    .uniform_work_group_size: 1
    .uses_dynamic_stack: false
    .vgpr_count:     58
    .vgpr_spill_count: 0
    .wavefront_size: 64
  - .agpr_count:     0
    .args:
      - .actual_access:  read_only
        .address_space:  global
        .offset:         0
        .size:           8
        .value_kind:     global_buffer
      - .actual_access:  write_only
        .address_space:  global
        .offset:         8
        .size:           8
        .value_kind:     global_buffer
      - .actual_access:  write_only
        .address_space:  global
        .offset:         16
        .size:           8
        .value_kind:     global_buffer
    .group_segment_fixed_size: 4176
    .kernarg_segment_align: 8
    .kernarg_segment_size: 24
    .language:       OpenCL C
    .language_version:
      - 2
      - 0
    .max_flat_workgroup_size: 1024
    .name:           _Z6sort_kPKiPiS1_
    .private_segment_fixed_size: 0
    .sgpr_count:     102
    .sgpr_spill_count: 0
    .symbol:         _Z6sort_kPKiPiS1_.kd
    .uniform_work_group_size: 1
    .uses_dynamic_stack: false
    .vgpr_count:     50
    .vgpr_spill_count: 0
    .wavefront_size: 64
  - .agpr_count:     0
    .args:
      - .offset:         0
        .size:           272
        .value_kind:     by_value
      - .actual_access:  read_only
        .address_space:  global
        .offset:         272
        .size:           8
        .value_kind:     global_buffer
      - .actual_access:  read_only
        .address_space:  global
        .offset:         280
        .size:           8
        .value_kind:     global_buffer
      - .actual_access:  read_only
        .address_space:  global
        .offset:         288
        .size:           8
        .value_kind:     global_buffer
      - .actual_access:  read_only
        .address_space:  global
        .offset:         296
        .size:           8
        .value_kind:     global_buffer
      - .actual_access:  read_only
        .address_space:  global
        .offset:         304
        .size:           8
        .value_kind:     global_buffer
      - .actual_access:  read_only
        .address_space:  global
        .offset:         312
        .size:           8
        .value_kind:     global_buffer
      - .actual_access:  read_only
        .address_space:  global
        .offset:         320
        .size:           8
        .value_kind:     global_buffer
      - .actual_access:  write_only
        .address_space:  global
        .offset:         328
        .size:           8
        .value_kind:     global_buffer
      - .actual_access:  write_only
        .address_space:  global
        .offset:         336
        .size:           8
        .value_kind:     global_buffer
      - .actual_access:  write_only
        .address_space:  global
        .offset:         344
        .size:           8
        .value_kind:     global_buffer
    .group_segment_fixed_size: 16640
    .kernarg_segment_align: 8
    .kernarg_segment_size: 352
    .language:       OpenCL C
    .language_version:
      - 2
      - 0
    .max_flat_workgroup_size: 256
    .name:           _Z5pre_k7CvtArgsPKiS1_PKfS3_S3_S3_S3_PfPDF16_S4_
    .private_segment_fixed_size: 0
    .sgpr_count:     24
    .sgpr_spill_count: 0
    .symbol:         _Z5pre_k7CvtArgsPKiS1_PKfS3_S3_S3_S3_PfPDF16_S4_.kd
    .uniform_work_group_size: 1
    .uses_dynamic_stack: false
    .vgpr_count:     69
    .vgpr_spill_count: 0
    .wavefront_size: 64
  - .agpr_count:     0
    .args:
      - .actual_access:  read_only
        .address_space:  global
        .offset:         0
        .size:           8
        .value_kind:     global_buffer
      - .actual_access:  read_only
        .address_space:  global
        .offset:         8
        .size:           8
        .value_kind:     global_buffer
      - .actual_access:  read_only
        .address_space:  global
        .offset:         16
        .size:           8
        .value_kind:     global_buffer
      - .actual_access:  read_only
        .address_space:  global
        .offset:         24
        .size:           8
        .value_kind:     global_buffer
      - .actual_access:  write_only
        .address_space:  global
        .offset:         32
        .size:           8
        .value_kind:     global_buffer
      - .actual_access:  read_only
        .address_space:  global
        .offset:         40
        .size:           8
        .value_kind:     global_buffer
      - .offset:         48
        .size:           4
        .value_kind:     by_value
      - .actual_access:  write_only
        .address_space:  global
        .offset:         56
        .size:           8
        .value_kind:     global_buffer
    .group_segment_fixed_size: 133120
    .kernarg_segment_align: 8
    .kernarg_segment_size: 64
    .language:       OpenCL C
    .language_version:
      - 2
      - 0
    .max_flat_workgroup_size: 512
    .name:           _Z6attn_kPKDF16_S0_S0_PKfPDF16_PK15HIP_vector_typeIfLj4EEiPf
    .private_segment_fixed_size: 0
    .sgpr_count:     102
    .sgpr_spill_count: 0
    .symbol:         _Z6attn_kPKDF16_S0_S0_PKfPDF16_PK15HIP_vector_typeIfLj4EEiPf.kd
    .uniform_work_group_size: 1
    .uses_dynamic_stack: false
    .vgpr_count:     119
    .vgpr_spill_count: 0
    .wavefront_size: 64
  - .agpr_count:     0
    .args:
      - .actual_access:  read_only
        .address_space:  global
        .offset:         0
        .size:           8
        .value_kind:     global_buffer
      - .actual_access:  read_only
        .address_space:  global
        .offset:         8
        .size:           8
        .value_kind:     global_buffer
      - .actual_access:  read_only
        .address_space:  global
        .offset:         16
        .size:           8
        .value_kind:     global_buffer
      - .actual_access:  read_only
        .address_space:  global
        .offset:         24
        .size:           8
        .value_kind:     global_buffer
      - .actual_access:  write_only
        .address_space:  global
        .offset:         32
        .size:           8
        .value_kind:     global_buffer
      - .actual_access:  read_only
        .address_space:  global
        .offset:         40
        .size:           8
        .value_kind:     global_buffer
      - .actual_access:  read_only
        .address_space:  global
        .offset:         48
        .size:           8
        .value_kind:     global_buffer
      - .actual_access:  write_only
        .address_space:  global
        .offset:         56
        .size:           8
        .value_kind:     global_buffer
      - .actual_access:  read_only
        .address_space:  global
        .offset:         64
        .size:           8
        .value_kind:     global_buffer
      - .offset:         72
        .size:           4
        .value_kind:     by_value
      - .actual_access:  read_only
        .address_space:  global
        .offset:         80
        .size:           8
        .value_kind:     global_buffer
      - .offset:         88
        .size:           4
        .value_kind:     by_value
      - .actual_access:  write_only
        .address_space:  global
        .offset:         96
        .size:           8
        .value_kind:     global_buffer
    .group_segment_fixed_size: 7168
    .kernarg_segment_align: 8
    .kernarg_segment_size: 104
    .language:       OpenCL C
    .language_version:
      - 2
      - 0
    .max_flat_workgroup_size: 256
    .name:           _Z9tail_up_kPKfPKiS0_S0_PfS0_S2_S3_PK15HIP_vector_typeIfLj4EEiS7_iS3_
    .private_segment_fixed_size: 0
    .sgpr_count:     72
    .sgpr_spill_count: 0
    .symbol:         _Z9tail_up_kPKfPKiS0_S0_PfS0_S2_S3_PK15HIP_vector_typeIfLj4EEiS7_iS3_.kd
    .uniform_work_group_size: 1
    .uses_dynamic_stack: false
    .vgpr_count:     114
    .vgpr_spill_count: 0
    .wavefront_size: 64
  - .agpr_count:     0
    .args:
      - .actual_access:  read_only
        .address_space:  global
        .offset:         0
        .size:           8
        .value_kind:     global_buffer
      - .offset:         8
        .size:           4
        .value_kind:     by_value
      - .actual_access:  read_only
        .address_space:  global
        .offset:         16
        .size:           8
        .value_kind:     global_buffer
      - .actual_access:  read_only
        .address_space:  global
        .offset:         24
        .size:           8
        .value_kind:     global_buffer
      - .actual_access:  read_only
        .address_space:  global
        .offset:         32
        .size:           8
        .value_kind:     global_buffer
      - .actual_access:  read_only
        .address_space:  global
        .offset:         40
        .size:           8
        .value_kind:     global_buffer
      - .actual_access:  write_only
        .address_space:  global
        .offset:         48
        .size:           8
        .value_kind:     global_buffer
    .group_segment_fixed_size: 0
    .kernarg_segment_align: 8
    .kernarg_segment_size: 56
    .language:       OpenCL C
    .language_version:
      - 2
      - 0
    .max_flat_workgroup_size: 512
    .name:           _Z9tail_ln_kPKfiS0_S0_S0_S0_Pf
    .private_segment_fixed_size: 0
    .sgpr_count:     22
    .sgpr_spill_count: 0
    .symbol:         _Z9tail_ln_kPKfiS0_S0_S0_S0_Pf.kd
    .uniform_work_group_size: 1
    .uses_dynamic_stack: false
    .vgpr_count:     48
    .vgpr_spill_count: 0
    .wavefront_size: 64
  - .agpr_count:     0
    .args:
      - .actual_access:  read_only
        .address_space:  global
        .offset:         0
        .size:           8
        .value_kind:     global_buffer
      - .actual_access:  read_only
        .address_space:  global
        .offset:         8
        .size:           8
        .value_kind:     global_buffer
      - .actual_access:  read_only
        .address_space:  global
        .offset:         16
        .size:           8
        .value_kind:     global_buffer
      - .actual_access:  read_only
        .address_space:  global
        .offset:         24
        .size:           8
        .value_kind:     global_buffer
      - .actual_access:  read_only
        .address_space:  global
        .offset:         32
        .size:           8
        .value_kind:     global_buffer
      - .actual_access:  read_only
        .address_space:  global
        .offset:         40
        .size:           8
        .value_kind:     global_buffer
      - .actual_access:  write_only
        .address_space:  global
        .offset:         48
        .size:           8
        .value_kind:     global_buffer
      - .actual_access:  write_only
        .address_space:  global
        .offset:         56
        .size:           8
        .value_kind:     global_buffer
    .group_segment_fixed_size: 47872
    .kernarg_segment_align: 8
    .kernarg_segment_size: 64
    .language:       OpenCL C
    .language_version:
      - 2
      - 0
    .max_flat_workgroup_size: 256
    .name:           _Z6pool_kPKfS0_S0_S0_S0_S0_PfS1_
    .private_segment_fixed_size: 0
    .sgpr_count:     102
    .sgpr_spill_count: 0
    .symbol:         _Z6pool_kPKfS0_S0_S0_S0_S0_PfS1_.kd
    .uniform_work_group_size: 1
    .uses_dynamic_stack: false
    .vgpr_count:     222
    .vgpr_spill_count: 0
    .wavefront_size: 64
  - .agpr_count:     0
    .args:
      - .actual_access:  read_only
        .address_space:  global
        .offset:         0
        .size:           8
        .value_kind:     global_buffer
      - .actual_access:  read_only
        .address_space:  global
        .offset:         8
        .size:           8
        .value_kind:     global_buffer
      - .actual_access:  read_only
        .address_space:  global
        .offset:         16
        .size:           8
        .value_kind:     global_buffer
      - .actual_access:  read_only
        .address_space:  global
        .offset:         24
        .size:           8
        .value_kind:     global_buffer
      - .actual_access:  read_only
        .address_space:  global
        .offset:         32
        .size:           8
        .value_kind:     global_buffer
      - .actual_access:  read_only
        .address_space:  global
        .offset:         40
        .size:           8
        .value_kind:     global_buffer
      - .actual_access:  write_only
        .address_space:  global
        .offset:         48
        .size:           8
        .value_kind:     global_buffer
    .group_segment_fixed_size: 16
    .kernarg_segment_align: 8
    .kernarg_segment_size: 56
    .language:       OpenCL C
    .language_version:
      - 2
      - 0
    .max_flat_workgroup_size: 256
    .name:           _Z8final2_kPKfS0_S0_S0_S0_S0_Pf
    .private_segment_fixed_size: 0
    .sgpr_count:     52
    .sgpr_spill_count: 0
    .symbol:         _Z8final2_kPKfS0_S0_S0_S0_S0_Pf.kd
    .uniform_work_group_size: 1
    .uses_dynamic_stack: false
    .vgpr_count:     67
    .vgpr_spill_count: 0
    .wavefront_size: 64
  - .agpr_count:     0
    .args:
      - .actual_access:  read_only
        .address_space:  global
        .offset:         0
        .size:           8
        .value_kind:     global_buffer
      - .offset:         8
        .size:           4
        .value_kind:     by_value
      - .actual_access:  read_only
        .address_space:  global
        .offset:         16
        .size:           8
        .value_kind:     global_buffer
      - .actual_access:  read_only
        .address_space:  global
        .offset:         24
        .size:           8
        .value_kind:     global_buffer
      - .actual_access:  read_only
        .address_space:  global
        .offset:         32
        .size:           8
        .value_kind:     global_buffer
      - .actual_access:  read_only
        .address_space:  global
        .offset:         40
        .size:           8
        .value_kind:     global_buffer
      - .actual_access:  write_only
        .address_space:  global
        .offset:         48
        .size:           8
        .value_kind:     global_buffer
    .group_segment_fixed_size: 0
    .kernarg_segment_align: 8
    .kernarg_segment_size: 56
    .language:       OpenCL C
    .language_version:
      - 2
      - 0
    .max_flat_workgroup_size: 512
    .name:           _Z7final_kPKfiS0_S0_S0_S0_Pf
    .private_segment_fixed_size: 0
    .sgpr_count:     36
    .sgpr_spill_count: 0
    .symbol:         _Z7final_kPKfiS0_S0_S0_S0_Pf.kd
    .uniform_work_group_size: 1
    .uses_dynamic_stack: false
    .vgpr_count:     20
    .vgpr_spill_count: 0
    .wavefront_size: 64
  - .agpr_count:     0
    .args:
      - .offset:         0
        .size:           136
        .value_kind:     by_value
    .group_segment_fixed_size: 114688
    .kernarg_segment_align: 8
    .kernarg_segment_size: 136
    .language:       OpenCL C
    .language_version:
      - 2
      - 0
    .max_flat_workgroup_size: 512
    .name:           _Z7gemm2_kILi0ELi3ELi1EEv5GArgs
    .private_segment_fixed_size: 0
    .sgpr_count:     102
    .sgpr_spill_count: 0
    .symbol:         _Z7gemm2_kILi0ELi3ELi1EEv5GArgs.kd
    .uniform_work_group_size: 1
    .uses_dynamic_stack: false
    .vgpr_count:     188
    .vgpr_spill_count: 0
    .wavefront_size: 64
  - .agpr_count:     0
    .args:
      - .offset:         0
        .size:           136
        .value_kind:     by_value
    .group_segment_fixed_size: 131072
    .kernarg_segment_align: 8
    .kernarg_segment_size: 136
    .language:       OpenCL C
    .language_version:
      - 2
      - 0
    .max_flat_workgroup_size: 512
    .name:           _Z6gemm_kILi1ELi128ELi4ELi8EEv5GArgs
    .private_segment_fixed_size: 0
    .sgpr_count:     102
    .sgpr_spill_count: 0
    .symbol:         _Z6gemm_kILi1ELi128ELi4ELi8EEv5GArgs.kd
    .uniform_work_group_size: 1
    .uses_dynamic_stack: false
    .vgpr_count:     76
    .vgpr_spill_count: 0
    .wavefront_size: 64
  - .agpr_count:     0
    .args:
      - .offset:         0
        .size:           136
        .value_kind:     by_value
    .group_segment_fixed_size: 81920
    .kernarg_segment_align: 8
    .kernarg_segment_size: 136
    .language:       OpenCL C
    .language_version:
      - 2
      - 0
    .max_flat_workgroup_size: 256
    .name:           _Z6gemm_kILi2ELi128ELi2ELi4EEv5GArgs
    .private_segment_fixed_size: 0
    .sgpr_count:     102
    .sgpr_spill_count: 0
    .symbol:         _Z6gemm_kILi2ELi128ELi2ELi4EEv5GArgs.kd
    .uniform_work_group_size: 1
    .uses_dynamic_stack: false
    .vgpr_count:     196
    .vgpr_spill_count: 0
    .wavefront_size: 64
  - .agpr_count:     0
    .args:
      - .offset:         0
        .size:           136
        .value_kind:     by_value
    .group_segment_fixed_size: 98304
    .kernarg_segment_align: 8
    .kernarg_segment_size: 136
    .language:       OpenCL C
    .language_version:
      - 2
      - 0
    .max_flat_workgroup_size: 512
    .name:           _Z7gemm2_kILi3ELi2ELi2EEv5GArgs
    .private_segment_fixed_size: 0
    .sgpr_count:     102
    .sgpr_spill_count: 0
    .symbol:         _Z7gemm2_kILi3ELi2ELi2EEv5GArgs.kd
    .uniform_work_group_size: 1
    .uses_dynamic_stack: false
    .vgpr_count:     172
    .vgpr_spill_count: 0
    .wavefront_size: 64
  - .agpr_count:     0
    .args:
      - .actual_access:  read_only
        .address_space:  global
        .offset:         0
        .size:           8
        .value_kind:     global_buffer
      - .actual_access:  read_only
        .address_space:  global
        .offset:         8
        .size:           8
        .value_kind:     global_buffer
      - .actual_access:  write_only
        .address_space:  global
        .offset:         16
        .size:           8
        .value_kind:     global_buffer
    .group_segment_fixed_size: 38912
    .kernarg_segment_align: 8
    .kernarg_segment_size: 24
    .language:       OpenCL C
    .language_version:
      - 2
      - 0
    .max_flat_workgroup_size: 256
    .name:           _Z7gemv8_kILi192ELi3072EEvPKfS1_Pf
    .private_segment_fixed_size: 0
    .sgpr_count:     102
    .sgpr_spill_count: 0
    .symbol:         _Z7gemv8_kILi192ELi3072EEvPKfS1_Pf.kd
    .uniform_work_group_size: 1
    .uses_dynamic_stack: false
    .vgpr_count:     128
    .vgpr_spill_count: 0
    .wavefront_size: 64
